# chunk items: the loop code copy now runs all five rounds (rounds 3 and 4 no longer execute their own cold code copies)
# speedup vs baseline: 1.0077x; 1.0077x over previous
; __device__ __forceinline__ void gdn_local_item(const Params& P, LAS unsigned char* lds, int item, int tid, bool defer, int& pend, unsigned& pend_fb) {
;     ...
;         for (int r = 0; r < 7; ++r) {
;             const int id = tid + 512 * r;
;             const int row = id / 48, rem = id - row * 48, part = rem >> 4, ck = rem & 15, s = n * 64 + row - 3;
;             pr[r] = (v4u){0u, 0u, 0u, 0u};
;             if (id < 67 * 48 && s >= 0) pr[r] = *(const v4u*)(QKV + (size_t)(b * SEQ + s) * 1536 + part * 512 + h * 128 + ck * 8);
;         }
; __global__ void __launch_bounds__(NWAVES * 64, 2) hybrid_fwd(Params P) {
;     ...
;               if (NWK == 224) {
;                   for (int r = 0; r < 3; ++r) { const int q = 224 * r + wk; gdn_local_item(P, lds, (q & 7) * 128 + (q >> 3), tid, r > 0, pend, pend_fb); }
;                   if (wk < 192) { const int q = 672 + wk; gdn_local_item(P, lds, (q & 7) * 128 + (q >> 3), tid, true, pend, pend_fb); }
;                   if (wk < 160) { const int q = 864 + wk; gdn_local_item(P, lds, (q & 7) * 128 + (q >> 3), tid, true, pend, pend_fb); }
.LBB0_481:
	s_or_b64 exec, exec, s[0:1]
	s_waitcnt lgkmcnt(0)
	s_barrier
	s_add_i32 s58, s58, 1
	s_cmpk_lt_i32 s2, 0xe0
	s_cselect_b32 s0, 4, 3
	s_cmpk_lt_i32 s2, 0xc0
	s_cselect_b32 s1, 1, 0
	s_add_i32 s0, s0, s1
	s_cmp_eq_u32 s58, s0
	s_cbranch_scc1 .LBB0_769
.LBB0_482:
	s_mul_i32 s0, s58, 0xe0
	s_cmp_eq_u32 s58, 4
	s_cselect_b32 s6, 32, 0
	s_sub_i32 s0, s0, s6
	v_readlane_b32 s6, v255, 10
	s_add_i32 s0, s0, s6
	s_ashr_i32 s66, s0, 3
	s_add_i32 s84, s66, s87
	v_mov_b32_e32 v91, v0
	s_lshl_b32 s0, s84, 4
	v_mul_hi_i32 v36, v91, s68
	s_and_b32 s23, s0, 0xffffe000
	s_lshl_b32 s0, s66, 6
	v_lshrrev_b32_e32 v38, 31, v36
	v_ashrrev_i32_e32 v3, 3, v36
	s_and_b32 s56, s0, 0x1fc0
	v_add_u32_e32 v3, v3, v38
	v_lshlrev_b32_e32 v44, 3, v91
	v_add_u32_e32 v8, s56, v3
	s_movk_i32 s0, 0xc90
	v_readlane_b32 s7, v255, 11
	s_bfe_u32 s22, s84, 0x20007
	v_and_b32_e32 v4, 0x78, v44
	v_cmp_gt_i32_e32 vcc, s0, v91
	v_cmp_lt_i32_e64 s[0:1], 2, v8
	v_readfirstlane_b32 s59, v91
	s_add_i32 s7, s23, -3
	s_lshl_b32 s6, s22, 7
	s_and_b64 s[8:9], vcc, s[0:1]
	v_lshlrev_b32_e32 v32, 1, v4
	v_mov_b32_e32 v4, v2
	v_mov_b32_e32 v5, v2
	v_mov_b32_e32 v6, v2
	v_mov_b32_e32 v7, v2
	s_and_saveexec_b64 s[0:1], s[8:9]
	s_cbranch_execz .LBB0_484
	v_mul_lo_u32 v3, v3, s69
	v_add_u32_e32 v6, s7, v8
	v_mov_b64_e32 v[4:5], s[60:61]
	v_add_lshl_u32 v3, v3, v91, 5
	v_mad_i64_i32 v[4:5], s[8:9], v6, s70, v[4:5]
	v_and_b32_e32 v6, 0xfffffe00, v3
	v_ashrrev_i32_e32 v7, 31, v6
	v_lshl_add_u64 v[4:5], v[6:7], 1, v[4:5]
	s_lshl_b32 s64, s6, 1
	v_lshl_add_u64 v[4:5], v[4:5], 0, s[64:65]
	v_mov_b32_e32 v33, v2
	v_lshl_add_u64 v[4:5], v[4:5], 0, v[32:33]
	global_load_dwordx4 v[4:7], v[4:5], off

; __global__ void __launch_bounds__(NWAVES * 64, 2) hybrid_fwd(Params P) {
;     ...
;               if (NWK == 224) {
;                   for (int r = 0; r < 3; ++r) { const int q = 224 * r + wk; gdn_local_item(P, lds, (q & 7) * 128 + (q >> 3), tid, r > 0, pend, pend_fb); }
;                   if (wk < 192) { const int q = 672 + wk; gdn_local_item(P, lds, (q & 7) * 128 + (q >> 3), tid, true, pend, pend_fb); }
;                   if (wk < 160) { const int q = 864 + wk; gdn_local_item(P, lds, (q & 7) * 128 + (q >> 3), tid, true, pend, pend_fb); }
.LBB0_768:
	s_mov_b32 s62, s84
	v_mov_b32_e32 v1, v3
	s_add_i32 s58, s58, 1
	s_cmpk_lt_i32 s2, 0xe0
	s_cselect_b32 s0, 4, 3
	s_cmpk_lt_i32 s2, 0xc0
	s_cselect_b32 s1, 1, 0
	s_add_i32 s0, s0, s1
	s_cmp_eq_u32 s58, s0
	s_cbranch_scc0 .LBB0_482
.LBB0_769:
	s_branch .LBB0_811

; __device__ __forceinline__ void gdn_local_item(const Params& P, LAS unsigned char* lds, int item, int tid, bool defer, int& pend, unsigned& pend_fb) {
;     ...
;         for (int r = 0; r < 7; ++r) {
;             const int id = tid + 512 * r;
;             const int row = id / 48, rem = id - row * 48, part = rem >> 4, ck = rem & 15, s = n * 64 + row - 3;
;             pr[r] = (v4u){0u, 0u, 0u, 0u};
;             if (id < 67 * 48 && s >= 0) pr[r] = *(const v4u*)(QKV + (size_t)(b * SEQ + s) * 1536 + part * 512 + h * 128 + ck * 8);
;         }
; __global__ void __launch_bounds__(NWAVES * 64, 2) hybrid_fwd(Params P) {
;     ...
;                   if (wk < 192) { const int q = 672 + wk; gdn_local_item(P, lds, (q & 7) * 128 + (q >> 3), tid, true, pend, pend_fb); }
	v_mov_b32_e32 v84, v0
	s_mov_b32 s8, 0x2aaaaaab
	s_add_i32 s0, s2, 0x280
	s_lshr_b32 s1, s0, 3
	v_mul_hi_i32 v3, v84, s8
	s_lshl_b32 s0, s0, 3
	v_lshrrev_b32_e32 v4, 31, v3
	v_ashrrev_i32_e32 v3, 3, v3
	s_add_i32 s64, s87, s1
	s_and_b32 s29, s0, 0x1fc0
	v_add_u32_e32 v3, v3, v4
	s_lshl_b32 s1, s64, 4
	v_lshlrev_b32_e32 v43, 3, v84
	v_add_u32_e32 v4, s29, v3
	s_movk_i32 s0, 0xc90
	s_bfe_u32 s22, s64, 0x20007
	s_and_b32 s23, s1, 0x7fffe000
	v_and_b32_e32 v5, 0x78, v43
	v_cmp_gt_i32_e32 vcc, s0, v84
	v_cmp_lt_i32_e64 s[0:1], 2, v4
	s_add_i32 s20, s23, -3
	s_lshl_b32 s58, s22, 7
	s_mov_b32 s7, 0
	v_readfirstlane_b32 s28, v84
	v_mov_b32_e32 v2, 0
	s_and_b64 s[10:11], vcc, s[0:1]
	v_lshlrev_b32_e32 v32, 1, v5
	v_mov_b32_e32 v6, 0
	v_mov_b32_e32 v7, 0
	v_mov_b32_e32 v8, 0
	v_mov_b32_e32 v9, 0
	s_and_saveexec_b64 s[0:1], s[10:11]
	s_mov_b32 s68, s88
	s_cbranch_execz .LBB0_772
	s_movk_i32 s6, 0xffd0
	v_mul_lo_u32 v3, v3, s6
	v_add_u32_e32 v6, s20, v4
	s_movk_i32 s6, 0xc00
	v_mov_b64_e32 v[4:5], s[60:61]
	v_add_lshl_u32 v3, v3, v84, 5
	v_mad_i64_i32 v[4:5], s[10:11], v6, s6, v[4:5]
	v_and_b32_e32 v6, 0xfffffe00, v3
	v_ashrrev_i32_e32 v7, 31, v6
	v_lshl_add_u64 v[4:5], v[6:7], 1, v[4:5]
	s_lshl_b32 s6, s58, 1
	v_lshl_add_u64 v[4:5], v[4:5], 0, s[6:7]
	v_mov_b32_e32 v33, 0
	v_lshl_add_u64 v[4:5], v[4:5], 0, v[32:33]
	global_load_dwordx4 v[6:9], v[4:5], off

; __global__ void __launch_bounds__(NWAVES * 64, 2) hybrid_fwd(Params P) {
;     ...
;                   if (wk < 160) { const int q = 864 + wk; gdn_local_item(P, lds, (q & 7) * 128 + (q >> 3), tid, true, pend, pend_fb); }
;               } else
;               for (int q = wk; q < 1024; q += NWK) gdn_local_item(P, lds, (q & 7) * 128 + (q >> 3), tid, q >= NWK, pend, pend_fb);
;               if (pend >= 0) { asm volatile("s_waitcnt vmcnt(0)" ::: "memory"); __syncthreads();
.LBB0_811:
	s_mov_b32 s64, s62
	s_mov_b32 s68, s88


